# 8 sub-queues, 2 items per claim
# baseline (speedup 1.0000x reference)
; #define LAS __attribute__((address_space(3)))
; DI kptr_t kargs_now() { kptr_t p = (kptr_t)__builtin_amdgcn_kernarg_segment_ptr(); asm volatile("" : "+s"(p)); return p; }
; #define RI_NEXT(D_) do { if (q.cnt == 8) { int b_ = 0; if (F.lane == 0) b_ = (int)__hip_atomic_fetch_add(qctr, 8u, __ATOMIC_RELAXED, __HIP_MEMORY_SCOPE_AGENT); q.base = __builtin_amdgcn_readfirstlane(b_); q.cnt = 0; } \
;         D_ = decode_item(KA, F.ws, kind, q.base + q.cnt); ++q.cnt; } while (0)
; DI void run_items1(Frame& F, int kind, int quota, QState& q) {
;     const kptr_t KA = kargs_now();
;     LAS float* scr = (LAS float*)(F.lds + F.wave * 16384);
;     unsigned* qctr = F.ctl + CW_QUEUE + 64 * kind;
;     ...
;     if (quota == 0) return;
;     TItem d; RI_NEXT(d); if (!d.valid) return;
; DI void phase_attn(Frame& F, int l) {
;     ...
;     QState cq; cq.base = 0; cq.cnt = 8;
;     constexpr int SLOT_ITEMS = 3;
;     if (F.bid & 1) { __syncthreads(); run_items1(F, 1 + l, SLOT_ITEMS, cq); }
.LBB0_398:
	v_readlane_b32 s8, v255, 14
	v_readlane_b32 s4, v253, 8
	s_lshl_b32 s58, s8, 6
	v_readlane_b32 s6, v253, 10
	v_readlane_b32 s7, v253, 11
	s_lshl_b64 s[0:1], s[58:59], 2
	s_mov_b64 s[2:3], s[6:7]
	s_add_u32 s0, s2, s0
	s_addc_u32 s1, s3, s1
	v_readlane_b32 s9, v255, 15
	s_add_u32 s12, s0, 0x8100
	s_addc_u32 s13, s1, 0
	v_readlane_b32 s100, v253, 29
	s_lshr_b32 s100, s100, 1
	s_and_b32 s100, s100, 7
	s_lshl_b32 s0, s100, 8
	s_mul_i32 s1, s8, 0x700
	s_add_i32 s0, s0, s1
	s_add_i32 s0, s0, 0xb00
	s_add_u32 s12, s12, s0
	s_addc_u32 s13, s13, 0
	s_lshl_b64 s[0:1], s[8:9], 25
	v_writelane_b32 v255, s0, 16
	s_lshl_b64 s[62:63], s[8:9], 5
	s_lshl_b32 s2, s8, 20
	v_writelane_b32 v255, s1, 17
	s_mov_b32 s3, s59
	v_readlane_b32 s0, v253, 33
	v_writelane_b32 v255, s2, 18
	s_add_u32 s76, s0, s2
	v_readlane_b32 s0, v253, 34
	v_writelane_b32 v255, s3, 19
	s_addc_u32 s77, s0, 0
	s_lshl_b64 s[20:21], s[8:9], 21
	s_lshl_b64 s[0:1], s[8:9], 20
	v_readlane_b32 s2, v253, 35
	s_add_u32 s22, s2, s0
	v_readlane_b32 s2, v253, 36
	s_addc_u32 s23, s2, s1
	v_readlane_b32 s2, v253, 37
	s_add_u32 s24, s2, s0
	v_readlane_b32 s0, v253, 38
	s_addc_u32 s25, s0, s1
	s_lshl_b64 s[26:27], s[8:9], 24
	v_readlane_b32 s0, v253, 39
	s_add_u32 s14, s0, s44
	v_readlane_b32 s0, v253, 40
	s_addc_u32 s15, s0, s45
	s_mov_b32 s0, -1
	s_mov_b32 s95, 0
	v_mbcnt_lo_u32_b32 v0, s0, 0
	v_mbcnt_hi_u32_b32 v186, s0, v0
	v_readlane_b32 s0, v253, 29
	s_mov_b32 s51, s0
	s_mov_b64 s[30:31], s[70:71]
	s_bitcmp0_b32 s51, 0
	s_mov_b32 s63, 2
	v_readlane_b32 s5, v253, 9
	v_readlane_b32 s1, v253, 30
	s_cbranch_scc1 .LBB0_472
	s_mov_b64 s[6:7], s[70:71]
	v_mov_b32_e32 v0, 0
	v_cmp_eq_u32_e64 s[4:5], 0, v186
	s_waitcnt vmcnt(63) expcnt(7) lgkmcnt(15)
	s_barrier
	s_and_saveexec_b64 s[2:3], s[4:5]
	s_cbranch_execz .LBB0_403
	s_mov_b64 s[10:11], exec
	v_mbcnt_lo_u32_b32 v0, s10, 0
	v_mbcnt_hi_u32_b32 v0, s11, v0
	v_cmp_eq_u32_e32 vcc, 0, v0
	s_and_saveexec_b64 s[8:9], vcc
	s_cbranch_execz .LBB0_402
	s_bcnt1_i32_b64 s0, s[10:11]
	s_lshl_b32 s0, s0, 1
	v_mov_b32_e32 v2, s0
	global_atomic_add v2, v1, v2, s[12:13] sc0
